# DeltaNet recurrence: operand copies for the lane-half exchange as 64-bit moves
# speedup vs baseline: 1.0001x; 1.0001x over previous
.LBB0_799:
	s_ashr_i32 s4, s16, 1
	s_lshl_b32 s20, s4, 6
	s_and_b32 s17, s4, 3
	s_and_b32 s4, s20, 0xffffff00
	s_or_b32 s14, s4, s17
	s_ashr_i32 s15, s14, 31
	s_lshl_b64 s[4:5], s[14:15], 13
	v_readlane_b32 s6, v253, 22
	v_lshl_add_u64 v[20:21], v[134:135], 0, s[4:5]
	v_readlane_b32 s7, v253, 23
	s_add_u32 s4, s6, s4
	s_addc_u32 s5, s7, s5
	s_lshl_b32 s6, s16, 11
	s_and_b32 s6, s6, 0x800
	v_or_b32_e32 v36, s6, v132
	v_lshlrev_b32_e32 v2, 1, v132
	v_mov_b32_e32 v143, v3
	v_mov_b32_e32 v37, v3
	v_lshlrev_b32_e32 v36, 1, v36
	v_lshl_add_u64 v[16:17], v[20:21], 0, v[2:3]
	v_lshl_add_u64 v[32:33], v[20:21], 0, v[142:143]
	v_mov_b32_e32 v145, v3
	v_lshl_add_u64 v[38:39], s[4:5], 0, v[36:37]
	global_load_dwordx4 v[4:7], v[16:17], off
	global_load_dwordx4 v[8:11], v[16:17], off offset:32
	global_load_dwordx4 v[12:15], v[16:17], off offset:64
	v_lshl_add_u64 v[38:39], v[38:39], 0, v[144:145]
	global_load_dwordx4 v[16:19], v[16:17], off offset:96
	s_nop 0
	global_load_dwordx4 v[20:23], v[32:33], off
	global_load_dwordx4 v[24:27], v[32:33], off offset:32
	global_load_dwordx4 v[28:31], v[32:33], off offset:64
	s_nop 0
	global_load_dwordx4 v[32:35], v[32:33], off offset:96
	s_nop 0
	global_load_dwordx2 v[158:159], v[38:39], off
	global_load_dwordx2 v[154:155], v[38:39], off offset:16
	global_load_dwordx2 v[152:153], v[38:39], off offset:32
	global_load_dwordx2 v[150:151], v[38:39], off offset:48
	global_load_dwordx2 v[164:165], v[38:39], off offset:64
	global_load_dwordx2 v[162:163], v[38:39], off offset:80
	global_load_dwordx2 v[160:161], v[38:39], off offset:96
	global_load_dwordx2 v[156:157], v[38:39], off offset:112
	v_lshl_add_u64 v[146:147], v[138:139], 0, v[36:37]
	v_lshl_add_u64 v[148:149], v[140:141], 0, v[36:37]
	s_mov_b32 s15, 0
	s_waitcnt vmcnt(0)
	v_cndmask_b32_e32 v38, v4, v6, vcc
	ds_bpermute_b32 v38, v166, v38
	s_waitcnt lgkmcnt(0)
	v_cndmask_b32_e32 v92, v38, v4, vcc
	v_mov_b32_e32 v4, 0
	v_mov_b32_e32 v93, v5
	v_mov_b32_e32 v95, v7
	s_nop 1
	v_permlane32_swap_b32_e32 v93, v95
	s_nop 1
	v_cndmask_b32_e32 v94, v6, v38, vcc
	s_waitcnt lgkmcnt(0)
	v_mov_b64_e32 v[76:77], v[8:9]
	v_mov_b64_e32 v[78:79], v[10:11]
	s_nop 1
	v_permlane32_swap_b32_e32 v77, v79
	v_permlane32_swap_b32_e32 v76, v78
	s_nop 1
	s_waitcnt lgkmcnt(0)
	v_mov_b64_e32 v[84:85], v[12:13]
	v_mov_b64_e32 v[86:87], v[14:15]
	s_nop 1
	v_permlane32_swap_b32_e32 v85, v87
	v_permlane32_swap_b32_e32 v84, v86
	s_nop 1
	s_waitcnt lgkmcnt(0)
	v_mov_b64_e32 v[68:69], v[16:17]
	v_mov_b64_e32 v[70:71], v[18:19]
	s_nop 1
	v_permlane32_swap_b32_e32 v69, v71
	v_permlane32_swap_b32_e32 v68, v70
	s_nop 1
	s_waitcnt lgkmcnt(0)
	v_mov_b64_e32 v[96:97], v[20:21]
	v_mov_b64_e32 v[98:99], v[22:23]
	s_nop 1
	v_permlane32_swap_b32_e32 v97, v99
	v_permlane32_swap_b32_e32 v96, v98
	s_nop 1
	s_waitcnt lgkmcnt(0)
	v_mov_b64_e32 v[80:81], v[24:25]
	v_mov_b64_e32 v[82:83], v[26:27]
	s_nop 1
	v_permlane32_swap_b32_e32 v81, v83
	v_permlane32_swap_b32_e32 v80, v82
	s_nop 1
	s_waitcnt lgkmcnt(0)
	v_mov_b64_e32 v[88:89], v[28:29]
	v_mov_b64_e32 v[90:91], v[30:31]
	s_nop 1
	v_permlane32_swap_b32_e32 v89, v91
	v_permlane32_swap_b32_e32 v88, v90
	s_nop 1
	s_waitcnt lgkmcnt(0)
	v_mov_b64_e32 v[72:73], v[32:33]
	v_mov_b64_e32 v[74:75], v[34:35]
	s_nop 1
	v_permlane32_swap_b32_e32 v73, v75
	v_permlane32_swap_b32_e32 v72, v74
	s_nop 1
	v_mov_b32_e32 v5, v4
	v_mov_b32_e32 v6, v4
	v_mov_b32_e32 v7, v4
	v_mov_b32_e32 v8, v4
	v_mov_b32_e32 v9, v4
	v_mov_b32_e32 v10, v4
	v_mov_b32_e32 v11, v4
	v_mov_b32_e32 v12, v4
	v_mov_b32_e32 v13, v4
	v_mov_b32_e32 v14, v4
	v_mov_b32_e32 v15, v4
	v_mov_b32_e32 v16, v4
	v_mov_b32_e32 v17, v4
	v_mov_b32_e32 v18, v4
	v_mov_b32_e32 v19, v4
	v_mov_b32_e32 v20, v4
	v_mov_b32_e32 v21, v4
	v_mov_b32_e32 v22, v4
	v_mov_b32_e32 v23, v4
	v_mov_b32_e32 v24, v4
	v_mov_b32_e32 v25, v4
	v_mov_b32_e32 v26, v4
	v_mov_b32_e32 v27, v4
	v_mov_b32_e32 v28, v4
	v_mov_b32_e32 v29, v4
	v_mov_b32_e32 v30, v4
	v_mov_b32_e32 v31, v4
	v_mov_b32_e32 v32, v4
	v_mov_b32_e32 v33, v4
	v_mov_b32_e32 v34, v4
	v_mov_b32_e32 v35, v4
.LBB0_800:
	v_lshlrev_b32_e32 v36, 16, v158
	v_and_b32_e32 v37, 0xffff0000, v158
	v_lshlrev_b32_e32 v38, 16, v159
	v_and_b32_e32 v39, 0xffff0000, v159
	v_lshlrev_b32_e32 v40, 16, v154
	v_and_b32_e32 v41, 0xffff0000, v154
	v_lshlrev_b32_e32 v42, 16, v155
	v_and_b32_e32 v43, 0xffff0000, v155
	v_lshlrev_b32_e32 v44, 16, v152
	v_and_b32_e32 v45, 0xffff0000, v152
	v_lshlrev_b32_e32 v46, 16, v153
	v_and_b32_e32 v47, 0xffff0000, v153
	v_lshlrev_b32_e32 v48, 16, v150
	v_and_b32_e32 v49, 0xffff0000, v150
	v_lshlrev_b32_e32 v50, 16, v151
	v_and_b32_e32 v51, 0xffff0000, v151
	v_cvt_pk_bf16_f32 v116, -v20, -v21
	v_cvt_pk_bf16_f32 v117, -v22, -v23
	v_cvt_pk_bf16_f32 v118, -v24, -v25
	v_cvt_pk_bf16_f32 v119, -v26, -v27
	v_lshlrev_b32_e32 v52, 16, v164
	v_and_b32_e32 v53, 0xffff0000, v164
	v_mfma_f32_32x32x16_bf16 v[36:51], v[92:95], v[116:119], v[36:51]
	v_lshlrev_b32_e32 v54, 16, v165
	v_and_b32_e32 v55, 0xffff0000, v165
	v_lshlrev_b32_e32 v56, 16, v162
	v_and_b32_e32 v57, 0xffff0000, v162
	v_lshlrev_b32_e32 v58, 16, v163
	v_and_b32_e32 v59, 0xffff0000, v163
	v_lshlrev_b32_e32 v60, 16, v160
	v_and_b32_e32 v61, 0xffff0000, v160
	v_lshlrev_b32_e32 v62, 16, v161
	v_and_b32_e32 v63, 0xffff0000, v161
	v_lshlrev_b32_e32 v64, 16, v156
	v_and_b32_e32 v65, 0xffff0000, v156
	v_lshlrev_b32_e32 v66, 16, v157
	v_and_b32_e32 v67, 0xffff0000, v157
	s_add_i32 s18, s14, s15
	s_ashr_i32 s19, s18, 31
	v_mfma_f32_32x32x16_bf16 v[52:67], v[96:99], v[116:119], v[52:67]
	s_lshl_b64 s[4:5], s[18:19], 2
	v_cvt_pk_bf16_f32 v120, -v4, -v5
	v_cvt_pk_bf16_f32 v121, -v6, -v7
	v_cvt_pk_bf16_f32 v122, -v8, -v9
	v_cvt_pk_bf16_f32 v123, -v10, -v11
	s_add_u32 s8, s12, s4
	s_addc_u32 s9, s13, s5
	s_lshl_b64 s[6:7], s[18:19], 13
	v_mfma_f32_32x32x16_bf16 v[36:51], v[84:87], v[120:123], v[36:51]
	v_lshl_add_u64 v[96:97], v[136:137], 0, s[6:7]
	v_cvt_pk_bf16_f32 v124, -v28, -v29
	v_cvt_pk_bf16_f32 v125, -v30, -v31
	v_lshl_add_u64 v[150:151], v[96:97], 0, v[2:3]
	v_mfma_f32_32x32x16_bf16 v[52:67], v[88:91], v[120:123], v[52:67]
	v_cvt_pk_bf16_f32 v126, -v32, -v33
	global_load_dword v204, v3, s[8:9]
	v_lshl_add_u64 v[152:153], v[96:97], 0, v[142:143]
	global_load_dwordx4 v[96:99], v[150:151], off
	global_load_dwordx4 v[116:119], v[150:151], off offset:32
	s_add_i32 s4, s18, 4
	s_ashr_i32 s5, s4, 31
	s_lshl_b64 s[4:5], s[4:5], 13
	v_cvt_pk_bf16_f32 v127, -v34, -v35
	global_load_dwordx4 v[84:87], v[152:153], off
	global_load_dwordx4 v[128:131], v[152:153], off offset:32
	global_load_dwordx4 v[168:171], v[150:151], off offset:64
	global_load_dwordx4 v[172:175], v[150:151], off offset:96
	global_load_dwordx4 v[176:179], v[152:153], off offset:64
	global_load_dwordx4 v[180:183], v[152:153], off offset:96
	v_lshl_add_u64 v[150:151], v[134:135], 0, s[4:5]
	v_lshl_add_u64 v[88:89], v[146:147], 0, s[4:5]
	v_cvt_pk_bf16_f32 v92, -v12, -v13
	v_cvt_pk_bf16_f32 v93, -v14, -v15
	v_cvt_pk_bf16_f32 v94, -v16, -v17
	v_cvt_pk_bf16_f32 v95, -v18, -v19
	v_lshl_add_u64 v[120:121], v[150:151], 0, v[2:3]
	v_lshl_add_u64 v[196:197], v[150:151], 0, v[142:143]
	global_load_dwordx2 v[158:159], v[88:89], off
	global_load_dwordx2 v[154:155], v[88:89], off offset:16
	global_load_dwordx2 v[152:153], v[88:89], off offset:32
	v_mfma_f32_32x32x16_bf16 v[36:51], v[76:79], v[124:127], v[36:51]
	global_load_dwordx2 v[150:151], v[88:89], off offset:48
	global_load_dwordx2 v[164:165], v[88:89], off offset:64
	global_load_dwordx2 v[162:163], v[88:89], off offset:80
	global_load_dwordx2 v[160:161], v[88:89], off offset:96
	global_load_dwordx2 v[156:157], v[88:89], off offset:112
	global_load_dwordx4 v[76:79], v[120:121], off
	s_nop 0
	global_load_dwordx4 v[88:91], v[120:121], off offset:32
	v_cvt_pk_bf16_f32 v100, v20, v21
	v_cvt_pk_bf16_f32 v101, v22, v23
	v_cvt_pk_bf16_f32 v102, v4, v5
	v_cvt_pk_bf16_f32 v103, v6, v7
	v_cvt_pk_bf16_f32 v104, v24, v25
	v_cvt_pk_bf16_f32 v105, v26, v27
	v_mfma_f32_32x32x16_bf16 v[52:67], v[80:83], v[124:127], v[52:67]
	global_load_dwordx4 v[80:83], v[120:121], off offset:64
	s_nop 0
	global_load_dwordx4 v[120:123], v[120:121], off offset:96
	s_nop 0
	global_load_dwordx4 v[184:187], v[196:197], off
	global_load_dwordx4 v[188:191], v[196:197], off offset:32
	global_load_dwordx4 v[192:195], v[196:197], off offset:64
	s_nop 0
	global_load_dwordx4 v[196:199], v[196:197], off offset:96
	v_lshl_add_u64 v[206:207], v[148:149], 0, s[6:7]
	v_cvt_pk_bf16_f32 v106, v8, v9
	v_cvt_pk_bf16_f32 v107, v10, v11
	v_cvt_pk_bf16_f32 v108, v28, v29
	v_cvt_pk_bf16_f32 v109, v30, v31
	v_cvt_pk_bf16_f32 v110, v12, v13
	v_mfma_f32_32x32x16_bf16 v[36:51], v[68:71], v[92:95], v[36:51]
	v_cvt_pk_bf16_f32 v111, v14, v15
	v_cvt_pk_bf16_f32 v112, v32, v33
	v_cvt_pk_bf16_f32 v113, v34, v35
	v_cvt_pk_bf16_f32 v114, v16, v17
	v_cvt_pk_bf16_f32 v115, v18, v19
	global_store_dwordx2 v[206:207], v[100:101], off
	global_store_dwordx2 v[206:207], v[102:103], off offset:64
	global_store_dwordx2 v[206:207], v[104:105], off offset:16
	global_store_dwordx2 v[206:207], v[106:107], off offset:80
	global_store_dwordx2 v[206:207], v[108:109], off offset:32
	global_store_dwordx2 v[206:207], v[110:111], off offset:96
	global_store_dwordx2 v[206:207], v[112:113], off offset:48
	global_store_dwordx2 v[206:207], v[114:115], off offset:112
	v_mfma_f32_32x32x16_bf16 v[52:67], v[72:75], v[92:95], v[52:67]
	v_cvt_pk_bf16_f32 v36, v36, v37
	v_cvt_pk_bf16_f32 v37, v38, v39
	v_cvt_pk_bf16_f32 v39, v42, v43
	v_cvt_pk_bf16_f32 v42, v48, v49
	v_cvt_pk_bf16_f32 v38, v40, v41
	v_cvt_pk_bf16_f32 v40, v44, v45
	v_cvt_pk_bf16_f32 v43, v50, v51
	s_nop 4
	v_cvt_pk_bf16_f32 v52, v52, v53
	v_cvt_pk_bf16_f32 v53, v54, v55
	v_cvt_pk_bf16_f32 v54, v56, v57
	v_cvt_pk_bf16_f32 v44, v60, v61
	v_cvt_pk_bf16_f32 v45, v62, v63
	v_cvt_pk_bf16_f32 v41, v46, v47
	v_cvt_pk_bf16_f32 v46, v64, v65
	v_lshl_add_u64 v[208:209], v[146:147], 0, s[6:7]
	v_cvt_pk_bf16_f32 v55, v58, v59
	v_cvt_pk_bf16_f32 v47, v66, v67
	global_store_dwordx2 v[208:209], v[36:37], off
	global_store_dwordx2 v[208:209], v[52:53], off offset:64
	global_store_dwordx2 v[208:209], v[38:39], off offset:16
	global_store_dwordx2 v[208:209], v[54:55], off offset:80
	global_store_dwordx2 v[208:209], v[40:41], off offset:32
	global_store_dwordx2 v[208:209], v[44:45], off offset:96
	global_store_dwordx2 v[208:209], v[42:43], off offset:48
	global_store_dwordx2 v[208:209], v[46:47], off offset:112
	s_add_i32 s15, s15, 4
	s_cmpk_lg_i32 s15, 0xfc
	s_waitcnt vmcnt(40)
	v_pk_mul_f32 v[34:35], v[34:35], v[204:205] op_sel_hi:[1,0]
	s_waitcnt vmcnt(39)
	s_waitcnt vmcnt(38)
	v_pk_mul_f32 v[32:33], v[32:33], v[204:205] op_sel_hi:[1,0]
	v_pk_mul_f32 v[30:31], v[30:31], v[204:205] op_sel_hi:[1,0]
	v_pk_mul_f32 v[28:29], v[28:29], v[204:205] op_sel_hi:[1,0]
	s_waitcnt vmcnt(37)
	s_waitcnt vmcnt(35)
	s_waitcnt vmcnt(34)
	v_pk_mul_f32 v[26:27], v[26:27], v[204:205] op_sel_hi:[1,0]
	v_pk_mul_f32 v[24:25], v[24:25], v[204:205] op_sel_hi:[1,0]
	v_pk_mul_f32 v[22:23], v[22:23], v[204:205] op_sel_hi:[1,0]
	s_waitcnt vmcnt(23)
	v_pk_mul_f32 v[20:21], v[20:21], v[204:205] op_sel_hi:[1,0]
	v_pk_mul_f32 v[18:19], v[18:19], v[204:205] op_sel_hi:[1,0]
	v_pk_mul_f32 v[16:17], v[16:17], v[204:205] op_sel_hi:[1,0]
	s_waitcnt vmcnt(20)
	v_cndmask_b32_e32 v60, v120, v122, vcc
	v_cndmask_b32_e32 v61, v121, v123, vcc
	s_waitcnt vmcnt(19)
	v_cndmask_b32_e32 v62, v184, v186, vcc
	v_cndmask_b32_e32 v63, v185, v187, vcc
	v_pk_mul_f32 v[14:15], v[14:15], v[204:205] op_sel_hi:[1,0]
	v_pk_mul_f32 v[12:13], v[12:13], v[204:205] op_sel_hi:[1,0]
	v_pk_mul_f32 v[10:11], v[10:11], v[204:205] op_sel_hi:[1,0]
	v_pk_mul_f32 v[8:9], v[8:9], v[204:205] op_sel_hi:[1,0]
	v_pk_mul_f32 v[6:7], v[6:7], v[204:205] op_sel_hi:[1,0]
	v_pk_mul_f32 v[4:5], v[4:5], v[204:205] op_sel_hi:[1,0]
	ds_bpermute_b32 v145, v166, v60
	ds_bpermute_b32 v167, v166, v61
	ds_bpermute_b32 v203, v166, v62
	ds_bpermute_b32 v204, v166, v63
	s_waitcnt lgkmcnt(0)
	v_mov_b64_e32 v[48:49], v[96:97]
	v_mov_b64_e32 v[50:51], v[98:99]
	s_nop 1
	v_permlane32_swap_b32_e32 v49, v51
	v_permlane32_swap_b32_e32 v48, v50
	s_nop 1
	s_waitcnt lgkmcnt(0)
	v_mov_b64_e32 v[60:61], v[84:85]
	v_mov_b64_e32 v[62:63], v[86:87]
	s_nop 1
	v_permlane32_swap_b32_e32 v61, v63
	v_permlane32_swap_b32_e32 v60, v62
	s_nop 1
	v_mfma_f32_32x32x16_bf16 v[20:35], v[48:51], v[36:39], v[20:35]
	s_waitcnt lgkmcnt(0)
	v_mov_b64_e32 v[48:49], v[168:169]
	v_mov_b64_e32 v[50:51], v[170:171]
	s_nop 1
	v_permlane32_swap_b32_e32 v49, v51
	v_permlane32_swap_b32_e32 v48, v50
	s_nop 1
	v_mfma_f32_32x32x16_bf16 v[4:19], v[60:63], v[36:39], v[4:19]
	s_waitcnt lgkmcnt(0)
	v_mov_b64_e32 v[36:37], v[176:177]
	v_mov_b64_e32 v[38:39], v[178:179]
	s_nop 1
	v_permlane32_swap_b32_e32 v37, v39
	v_permlane32_swap_b32_e32 v36, v38
	s_nop 1
	v_mfma_f32_32x32x16_bf16 v[20:35], v[48:51], v[52:55], v[20:35]
	s_waitcnt vmcnt(18)
	v_mfma_f32_32x32x16_bf16 v[4:19], v[36:39], v[52:55], v[4:19]
	s_waitcnt vmcnt(17)
	v_mov_b64_e32 v[56:57], v[116:117]
	v_mov_b64_e32 v[58:59], v[118:119]
	s_nop 1
	v_permlane32_swap_b32_e32 v57, v59
	v_permlane32_swap_b32_e32 v56, v58
	s_nop 1
	s_waitcnt lgkmcnt(0)
	v_mov_b64_e32 v[64:65], v[128:129]
	v_mov_b64_e32 v[66:67], v[130:131]
	s_nop 1
	v_permlane32_swap_b32_e32 v65, v67
	v_permlane32_swap_b32_e32 v64, v66
	s_nop 1
	v_mfma_f32_32x32x16_bf16 v[20:35], v[56:59], v[40:43], v[20:35]
	v_mov_b64_e32 v[68:69], v[172:173]
	v_mov_b64_e32 v[70:71], v[174:175]
	s_nop 1
	v_permlane32_swap_b32_e32 v69, v71
	v_permlane32_swap_b32_e32 v68, v70
	s_nop 1
	s_waitcnt lgkmcnt(0)
	v_mov_b64_e32 v[60:61], v[180:181]
	v_mov_b64_e32 v[62:63], v[182:183]
	s_nop 1
	v_permlane32_swap_b32_e32 v61, v63
	v_permlane32_swap_b32_e32 v60, v62
	s_nop 1
	v_mfma_f32_32x32x16_bf16 v[4:19], v[64:67], v[40:43], v[4:19]
	s_waitcnt vmcnt(16)
	v_mov_b64_e32 v[128:129], v[76:77]
	v_mov_b64_e32 v[130:131], v[78:79]
	s_nop 1
	v_permlane32_swap_b32_e32 v129, v131
	v_permlane32_swap_b32_e32 v128, v130
	s_nop 1
	v_mfma_f32_32x32x16_bf16 v[20:35], v[68:71], v[44:47], v[20:35]
	s_waitcnt lgkmcnt(0)
	v_mov_b64_e32 v[112:113], v[88:89]
	v_mov_b64_e32 v[114:115], v[90:91]
	s_nop 1
	v_permlane32_swap_b32_e32 v113, v115
	v_permlane32_swap_b32_e32 v112, v114
	s_nop 1
	s_waitcnt lgkmcnt(0)
	v_mov_b64_e32 v[124:125], v[80:81]
	v_mov_b64_e32 v[126:127], v[82:83]
	s_nop 1
	v_permlane32_swap_b32_e32 v125, v127
	v_permlane32_swap_b32_e32 v124, v126
	s_nop 1
	v_mfma_f32_32x32x16_bf16 v[4:19], v[60:63], v[44:47], v[4:19]
	v_cndmask_b32_e32 v109, v167, v121, vcc
	v_cndmask_b32_e32 v108, v145, v120, vcc
	v_cndmask_b32_e32 v121, v204, v185, vcc
	v_cndmask_b32_e32 v120, v203, v184, vcc
	s_waitcnt lgkmcnt(0)
	v_mov_b64_e32 v[104:105], v[188:189]
	v_mov_b64_e32 v[106:107], v[190:191]
	s_nop 1
	v_permlane32_swap_b32_e32 v105, v107
	v_permlane32_swap_b32_e32 v104, v106
	s_nop 1
	s_waitcnt lgkmcnt(0)
	v_mov_b64_e32 v[116:117], v[192:193]
	v_mov_b64_e32 v[118:119], v[194:195]
	s_nop 1
	v_permlane32_swap_b32_e32 v117, v119
	v_permlane32_swap_b32_e32 v116, v118
	s_nop 1
	s_waitcnt lgkmcnt(0)
	v_mov_b64_e32 v[100:101], v[196:197]
	v_mov_b64_e32 v[102:103], v[198:199]
	s_nop 1
	v_permlane32_swap_b32_e32 v101, v103
	v_permlane32_swap_b32_e32 v100, v102
	s_nop 1
	v_cndmask_b32_e32 v111, v123, v167, vcc
	v_cndmask_b32_e32 v110, v122, v145, vcc
	v_cndmask_b32_e32 v123, v187, v204, vcc
	v_cndmask_b32_e32 v122, v186, v203, vcc
	v_mov_b64_e32 v[72:73], v[100:101]
	v_mov_b64_e32 v[88:89], v[116:117]
	v_mov_b64_e32 v[80:81], v[104:105]
	v_mov_b64_e32 v[96:97], v[120:121]
	v_mov_b64_e32 v[68:69], v[108:109]
	v_mov_b64_e32 v[84:85], v[124:125]
	v_mov_b64_e32 v[76:77], v[112:113]
	v_mov_b64_e32 v[92:93], v[128:129]
	v_mov_b64_e32 v[74:75], v[102:103]
	v_mov_b64_e32 v[90:91], v[118:119]
	v_mov_b64_e32 v[82:83], v[106:107]
	v_mov_b64_e32 v[98:99], v[122:123]
	v_mov_b64_e32 v[70:71], v[110:111]
	v_mov_b64_e32 v[86:87], v[126:127]
	v_mov_b64_e32 v[78:79], v[114:115]
	v_mov_b64_e32 v[94:95], v[130:131]
	s_cbranch_scc1 .LBB0_800
	v_cvt_pk_bf16_f32 v70, v20, v21
	v_cvt_pk_bf16_f32 v20, -v20, -v21
	v_cvt_pk_bf16_f32 v71, v22, v23
	v_cvt_pk_bf16_f32 v21, -v22, -v23
	v_cvt_pk_bf16_f32 v22, -v24, -v25
	v_lshlrev_b32_e32 v52, 16, v158
	v_and_b32_e32 v53, 0xffff0000, v158
	v_lshlrev_b32_e32 v54, 16, v159
	v_and_b32_e32 v55, 0xffff0000, v159
	v_lshlrev_b32_e32 v56, 16, v154
	v_and_b32_e32 v57, 0xffff0000, v154
	v_lshlrev_b32_e32 v58, 16, v155
	v_and_b32_e32 v59, 0xffff0000, v155
	v_lshlrev_b32_e32 v60, 16, v152
	v_and_b32_e32 v61, 0xffff0000, v152
	v_lshlrev_b32_e32 v62, 16, v153
	v_and_b32_e32 v63, 0xffff0000, v153
	v_lshlrev_b32_e32 v64, 16, v150
	v_and_b32_e32 v65, 0xffff0000, v150
	v_lshlrev_b32_e32 v66, 16, v151
	v_and_b32_e32 v67, 0xffff0000, v151
	v_cvt_pk_bf16_f32 v23, -v26, -v27
	v_lshlrev_b32_e32 v36, 16, v164
	v_and_b32_e32 v37, 0xffff0000, v164
	v_lshlrev_b32_e32 v38, 16, v165
	v_and_b32_e32 v39, 0xffff0000, v165
	v_lshlrev_b32_e32 v40, 16, v162
	v_and_b32_e32 v41, 0xffff0000, v162
	v_lshlrev_b32_e32 v42, 16, v163
	v_and_b32_e32 v43, 0xffff0000, v163
	v_lshlrev_b32_e32 v44, 16, v160
	v_and_b32_e32 v45, 0xffff0000, v160
	v_lshlrev_b32_e32 v46, 16, v161
	v_and_b32_e32 v47, 0xffff0000, v161
	v_lshlrev_b32_e32 v48, 16, v156
	v_and_b32_e32 v49, 0xffff0000, v156
	v_lshlrev_b32_e32 v50, 16, v157
	v_and_b32_e32 v51, 0xffff0000, v157
	v_mfma_f32_32x32x16_bf16 v[52:67], v[128:131], v[20:23], v[52:67]
	v_cvt_pk_bf16_f32 v72, v4, v5
	v_cvt_pk_bf16_f32 v4, -v4, -v5
	v_cvt_pk_bf16_f32 v73, v6, v7
	v_mfma_f32_32x32x16_bf16 v[36:51], v[120:123], v[20:23], v[36:51]
	v_cvt_pk_bf16_f32 v5, -v6, -v7
	v_cvt_pk_bf16_f32 v6, -v8, -v9
	v_cvt_pk_bf16_f32 v7, -v10, -v11
	s_or_b32 s4, s20, s17
	v_mfma_f32_32x32x16_bf16 v[52:67], v[124:127], v[4:7], v[52:67]
	s_or_b32 s4, s4, 0xfc
	s_ashr_i32 s5, s4, 31
	s_lshl_b64 s[14:15], s[4:5], 13
	v_lshl_add_u64 v[68:69], v[148:149], 0, s[14:15]
	global_store_dwordx2 v[68:69], v[70:71], off
	global_store_dwordx2 v[68:69], v[72:73], off offset:64
	v_cvt_pk_bf16_f32 v72, v8, v9
	v_mfma_f32_32x32x16_bf16 v[36:51], v[116:119], v[4:7], v[36:51]
	v_cvt_pk_bf16_f32 v4, -v28, -v29
	v_cvt_pk_bf16_f32 v5, -v30, -v31
	v_cvt_pk_bf16_f32 v6, -v32, -v33
	v_cvt_pk_bf16_f32 v7, -v34, -v35
	v_cvt_pk_bf16_f32 v8, -v12, -v13
	v_mfma_f32_32x32x16_bf16 v[52:67], v[112:115], v[4:7], v[52:67]
	v_cvt_pk_bf16_f32 v73, v10, v11
	v_cvt_pk_bf16_f32 v9, -v14, -v15
	v_cvt_pk_bf16_f32 v10, -v16, -v17
	v_mfma_f32_32x32x16_bf16 v[36:51], v[104:107], v[4:7], v[36:51]
	v_xor_b32_e32 v2, 0x80000000, v18
	v_xor_b32_e32 v11, 0x80000000, v19
	v_cvt_pk_bf16_f32 v11, v2, v11
	v_cvt_pk_bf16_f32 v70, v24, v25
	v_cvt_pk_bf16_f32 v71, v26, v27
	global_store_dwordx2 v[68:69], v[70:71], off offset:16
	global_store_dwordx2 v[68:69], v[72:73], off offset:80
	v_cvt_pk_bf16_f32 v70, v28, v29
	v_mfma_f32_32x32x16_bf16 v[52:67], v[108:111], v[8:11], v[52:67]
	v_cvt_pk_bf16_f32 v71, v30, v31
	v_cvt_pk_bf16_f32 v72, v12, v13
	v_cvt_pk_bf16_f32 v73, v14, v15
	global_store_dwordx2 v[68:69], v[70:71], off offset:32
	global_store_dwordx2 v[68:69], v[72:73], off offset:96
	v_cvt_pk_bf16_f32 v70, v32, v33
	v_cvt_pk_bf16_f32 v71, v34, v35
	v_lshl_add_u64 v[4:5], v[146:147], 0, s[14:15]
	v_mfma_f32_32x32x16_bf16 v[36:51], v[100:103], v[8:11], v[36:51]
	s_nop 2
	v_cvt_pk_bf16_f32 v6, v52, v53
	v_cvt_pk_bf16_f32 v7, v54, v55
	v_cvt_pk_bf16_f32 v72, v16, v17
	v_cvt_pk_bf16_f32 v73, v18, v19
	global_store_dwordx2 v[68:69], v[70:71], off offset:48
	global_store_dwordx2 v[68:69], v[72:73], off offset:112
	s_add_i32 s16, s16, s54
	s_cmp_lt_i32 s16, 64
	s_nop 0
	v_cvt_pk_bf16_f32 v8, v36, v37
	v_cvt_pk_bf16_f32 v9, v38, v39
	global_store_dwordx2 v[4:5], v[6:7], off
	global_store_dwordx2 v[4:5], v[8:9], off offset:64
	v_cvt_pk_bf16_f32 v6, v56, v57
	v_cvt_pk_bf16_f32 v7, v58, v59
	v_cvt_pk_bf16_f32 v8, v40, v41
	v_cvt_pk_bf16_f32 v9, v42, v43
	global_store_dwordx2 v[4:5], v[6:7], off offset:16
	global_store_dwordx2 v[4:5], v[8:9], off offset:80
	v_cvt_pk_bf16_f32 v6, v60, v61
	v_cvt_pk_bf16_f32 v7, v62, v63
	v_cvt_pk_bf16_f32 v8, v44, v45
	v_cvt_pk_bf16_f32 v9, v46, v47
	global_store_dwordx2 v[4:5], v[6:7], off offset:32
	global_store_dwordx2 v[4:5], v[8:9], off offset:96
	v_cvt_pk_bf16_f32 v6, v64, v65
	v_cvt_pk_bf16_f32 v7, v66, v67
	v_cvt_pk_bf16_f32 v8, v48, v49
	v_cvt_pk_bf16_f32 v9, v50, v51
	global_store_dwordx2 v[4:5], v[6:7], off offset:48
	global_store_dwordx2 v[4:5], v[8:9], off offset:112
	s_cbranch_scc1 .LBB0_799
